# defer2 with P2 unit split 7sp+5kv (WGs<128) vs 1sp+3kv+tile (WGs>=128)
# speedup vs baseline: 1.0016x; 1.0016x over previous
; #define LAS __attribute__((address_space(3)))
; __device__ __forceinline__ unsigned cvt_pk_bf16(float lo, float hi) { f32x2 v = {lo, hi}; bf16x2_t b = __builtin_convertvector(v, bf16x2_t); return __builtin_bit_cast(unsigned, b); }
; __device__ __forceinline__ void spatial_unit(Frame& F, const Args& a, int n, int g) {
;     LAS unsigned char* Wimg = F.lds; LAS unsigned char* Vimg = F.lds + 32768; LAS float* stats = (LAS float*)(F.lds + 65536);
;     const int t0 = n * 128, ch0 = g * 128, tid = F.tid, lane = F.lane, w = F.wave;
;     const bf16_t* V = (const bf16_t*)(F.ws + WS_V); const bf16_t* U = (const bf16_t*)(F.ws + WS_U); bf16_t* SG = (bf16_t*)(F.ws + WS_SG);
;     const float* vstat = (const float*)(F.ws + WS_VSTAT);
;     if (tid < 128) { const f32x4* p = (const f32x4*)(vstat + (size_t)(t0 + tid) * 32); float s = 0.f, q = 0.f;
; #pragma unroll
;         for (int j = 0; j < 8; ++j) { const f32x4 v = p[j]; s += v[0] + v[2]; q += v[1] + v[3]; }
;         const float mean = s * (1.f / GW), var = q * (1.f / GW) - mean * mean;
;         stats[2 * tid] = mean; stats[2 * tid + 1] = 1.0f / sqrtf(fmaxf(var, 0.f) + EPS); }
;     const float* ws_g = a.in[5] + (size_t)g * 128 * 128;
; #pragma unroll
;     for (int i = 0; i < 4; ++i) { const int id = tid + 512 * i, t = id >> 4, ch = id & 15;
;         const f32x4 x0 = *(const f32x4*)(ws_g + t * 128 + 8 * ch), x1 = *(const f32x4*)(ws_g + t * 128 + 8 * ch + 4);
;         float v[8] = {x0[0], x0[1], x0[2], x0[3], x1[0], x1[1], x1[2], x1[3]};
; #pragma unroll
;         for (int j = 0; j < 8; ++j) v[j] = (8 * ch + j <= t) ? v[j] : 0.f;
;         u32x4 o; o.x = cvt_pk_bf16(v[0], v[1]); o.y = cvt_pk_bf16(v[2], v[3]); o.z = cvt_pk_bf16(v[4], v[5]); o.w = cvt_pk_bf16(v[6], v[7]);
;         *(LAS u32x4*)(Wimg + off_b(t, ch)) = o; }
; __global__ void __launch_bounds__(NTHREADS, 2) mk_fwd(Args args) {
;     ...
;         if (MK_NSCAN == 0) for (int u = blockIdx.x; u < 1024; u += F.G) spatial_unit(F, args, u >> 3, u & 7);
.Lp2_body:
	s_waitcnt vmcnt(0)
	v_mov_b32_e32 v67, v0
	s_cmpk_gt_i32 s92, 0x3ff
	v_readfirstlane_b32 s0, v67
	s_cbranch_scc1 .LBB0_353
	v_ashrrev_i32_e32 v1, 4, v67
	v_lshlrev_b32_e32 v14, 2, v1
	v_and_b32_e32 v68, 15, v67
	v_and_b32_e32 v14, 12, v14
	v_bfe_u32 v78, v1, 2, 2
	v_bitop3_b32 v14, v14, v68, v78 bitop3:0x36
	v_lshl_add_u32 v81, v14, 4, 0
	v_add_u32_e32 v14, 0x200, v67
	v_ashrrev_i32_e32 v69, 4, v14
	v_lshlrev_b32_e32 v15, 2, v69
	v_and_b32_e32 v15, 12, v15
	v_bfe_u32 v16, v69, 2, 2
	v_bitop3_b32 v15, v15, v68, v16 bitop3:0x36
	v_add_u32_e32 v16, 0x400, v67
	v_ashrrev_i32_e32 v73, 4, v16
	v_lshlrev_b32_e32 v17, 2, v73
	s_load_dwordx8 s[72:79], s[96:97], 0x18
	v_and_b32_e32 v17, 12, v17
	v_bfe_u32 v18, v73, 2, 2
	v_bitop3_b32 v17, v17, v68, v18 bitop3:0x36
	v_add_u32_e32 v18, 0x600, v67
	v_lshlrev_b32_e32 v6, 3, v68
	v_ashrrev_i32_e32 v76, 4, v18
	v_mov_b32_e32 v2, 0
	v_cmp_gt_i32_e64 s[8:9], v6, v1
	v_cmp_lt_i32_e64 s[10:11], v6, v1
	v_or_b32_e32 v7, 2, v6
	v_or_b32_e32 v8, 3, v6
	v_or_b32_e32 v9, 4, v6
	v_or_b32_e32 v10, 5, v6
	v_or_b32_e32 v11, 6, v6
	v_or_b32_e32 v12, 7, v6
	v_cmp_gt_i32_e64 s[24:25], v6, v69
	v_cmp_lt_i32_e64 s[26:27], v6, v69
	v_cmp_gt_i32_e64 s[42:43], v6, v73
	v_cmp_lt_i32_e64 s[44:45], v6, v73
	v_cmp_gt_i32_e64 s[58:59], v6, v76
	v_cmp_lt_i32_e64 s[60:61], v6, v76
	v_lshlrev_b32_e32 v6, 2, v76
	s_waitcnt lgkmcnt(0)
; #define LAS __attribute__((address_space(3)))
; __device__ __forceinline__ void spatial_unit(Frame& F, const Args& a, int n, int g) {
;     LAS unsigned char* Wimg = F.lds; LAS unsigned char* Vimg = F.lds + 32768; LAS float* stats = (LAS float*)(F.lds + 65536);
;     const int t0 = n * 128, ch0 = g * 128, tid = F.tid, lane = F.lane, w = F.wave;
;     const bf16_t* V = (const bf16_t*)(F.ws + WS_V); const bf16_t* U = (const bf16_t*)(F.ws + WS_U); bf16_t* SG = (bf16_t*)(F.ws + WS_SG);
;     const float* vstat = (const float*)(F.ws + WS_VSTAT);
;     if (tid < 128) { const f32x4* p = (const f32x4*)(vstat + (size_t)(t0 + tid) * 32); float s = 0.f, q = 0.f;
; #pragma unroll
;         for (int j = 0; j < 8; ++j) { const f32x4 v = p[j]; s += v[0] + v[2]; q += v[1] + v[3]; }
;         const float mean = s * (1.f / GW), var = q * (1.f / GW) - mean * mean;
;         stats[2 * tid] = mean; stats[2 * tid + 1] = 1.0f / sqrtf(fmaxf(var, 0.f) + EPS); }
;     const float* ws_g = a.in[5] + (size_t)g * 128 * 128;
; #pragma unroll
;     for (int i = 0; i < 4; ++i) { const int id = tid + 512 * i, t = id >> 4, ch = id & 15;
;         const f32x4 x0 = *(const f32x4*)(ws_g + t * 128 + 8 * ch), x1 = *(const f32x4*)(ws_g + t * 128 + 8 * ch + 4);
;         float v[8] = {x0[0], x0[1], x0[2], x0[3], x1[0], x1[1], x1[2], x1[3]};
; #pragma unroll
;         for (int j = 0; j < 8; ++j) v[j] = (8 * ch + j <= t) ? v[j] : 0.f;
;         u32x4 o; o.x = cvt_pk_bf16(v[0], v[1]); o.y = cvt_pk_bf16(v[2], v[3]); o.z = cvt_pk_bf16(v[4], v[5]); o.w = cvt_pk_bf16(v[6], v[7]);
;         *(LAS u32x4*)(Wimg + off_b(t, ch)) = o; }
;     __syncthreads();
;     const float* lng = a.in[3]; const float* lnb = a.in[4];
;     {
;         u32x4 xv[4]; const int ch = tid & 15;
; #pragma unroll
;         for (int i = 0; i < 4; ++i) xv[i] = __builtin_nontemporal_load((const u32x4*)(V + (size_t)(t0 + (tid >> 4) + 32 * i) * GW + ch0 + 8 * ch));
;         const f32x4 g0 = *(const f32x4*)(lng + ch0 + 8 * ch), g1 = *(const f32x4*)(lng + ch0 + 8 * ch + 4), b0 = *(const f32x4*)(lnb + ch0 + 8 * ch), b1 = *(const f32x4*)(lnb + ch0 + 8 * ch + 4);
; __global__ void __launch_bounds__(NTHREADS, 2) mk_fwd(Args args) {
;     ...
;         if (MK_NSCAN == 0) for (int u = blockIdx.x; u < 1024; u += F.G) spatial_unit(F, args, u >> 3, u & 7);
	v_lshlrev_b32_e32 v4, 5, v68
	v_mov_b32_e32 v5, v2
	v_cmp_gt_i32_e64 s[12:13], v7, v1
	v_cmp_gt_i32_e64 s[28:29], v7, v69
	v_cmp_gt_i32_e64 s[46:47], v7, v73
	v_cmp_gt_i32_e64 s[62:63], v7, v76
	v_and_b32_e32 v6, 12, v6
	v_bfe_u32 v7, v76, 2, 2
	v_and_b32_e32 v3, 63, v67
	v_lshl_add_u64 v[46:47], s[76:77], 0, v[4:5]
	v_cmp_gt_i32_e64 s[18:19], v10, v1
	v_cmp_gt_i32_e64 s[36:37], v10, v69
	v_cmp_gt_i32_e64 s[52:53], v10, v73
	v_cmp_gt_i32_e64 s[68:69], v10, v76
	v_bitop3_b32 v6, v6, v68, v7 bitop3:0x36
	v_lshlrev_b32_e32 v44, 4, v68
	v_mov_b32_e32 v45, v2
	v_lshl_add_u64 v[50:51], s[72:73], 0, v[4:5]
	v_lshl_add_u64 v[52:53], s[74:75], 0, v[4:5]
	v_bfe_u32 v5, v67, 2, 2
	v_bfe_u32 v10, v67, 1, 5
	v_lshlrev_b32_e32 v77, 3, v67
	v_cmp_gt_i32_e64 s[16:17], v9, v1
	v_cmp_gt_i32_e64 s[34:35], v9, v69
	v_cmp_gt_i32_e64 s[50:51], v9, v73
	v_cmp_gt_i32_e64 s[66:67], v9, v76
	v_lshl_add_u32 v9, v6, 4, 0
	v_lshl_add_u64 v[6:7], s[94:95], 0, v[44:45]
	v_and_b32_e32 v10, 24, v10
	v_bfe_u32 v45, v3, 1, 1
	v_lshlrev_b32_e32 v3, 2, v5
	v_lshrrev_b32_e32 v19, 3, v67
	v_or_b32_e32 v18, v10, v5
	v_and_or_b32 v79, v19, 2, v3
	v_and_b32_e32 v19, 8, v77
	v_or_b32_e32 v10, 4, v10
	v_lshl_or_b32 v72, v18, 8, v19
	v_or_b32_e32 v18, v10, v5
	v_bfe_u32 v10, v10, 2, 2
	v_lshl_or_b32 v75, v18, 8, v19
	v_or_b32_e32 v18, v79, v45
	v_lshl_or_b32 v89, v18, 4, v72
	v_bitop3_b32 v18, v10, v45, v3 bitop3:0x36
	v_lshl_or_b32 v90, v18, 4, v75
	v_or_b32_e32 v18, 2, v45
	v_bitop3_b32 v18, v10, v18, v3 bitop3:0x36
	v_lshl_or_b32 v92, v18, 4, v75
	v_or_b32_e32 v18, 4, v45
	v_bitop3_b32 v18, v10, v18, v3 bitop3:0x36
	v_lshl_or_b32 v94, v18, 4, v75
	v_or_b32_e32 v18, 6, v45
	v_bitop3_b32 v18, v10, v18, v3 bitop3:0x36
	v_lshl_or_b32 v96, v18, 4, v75
	v_or_b32_e32 v18, 8, v45
	v_bitop3_b32 v18, v10, v18, v3 bitop3:0x36
	s_ashr_i32 s3, s0, 6
	v_bitop3_b32 v19, v45, v79, 2 bitop3:0x36
	v_lshl_or_b32 v98, v18, 4, v75
	v_or_b32_e32 v18, 10, v45
	s_movk_i32 s1, 0x80
	s_add_u32 s80, s94, 0x50600000
	v_lshl_or_b32 v91, v19, 4, v72
	v_bitop3_b32 v19, v45, v79, 4 bitop3:0x36
	v_bitop3_b32 v18, v10, v18, v3 bitop3:0x36
	v_cmp_gt_i32_e64 s[6:7], s1, v67
	s_addc_u32 s81, s95, 0
	v_lshl_or_b32 v93, v19, 4, v72
	v_bitop3_b32 v19, v45, v79, 6 bitop3:0x36
	v_lshl_or_b32 v100, v18, 4, v75
	v_or_b32_e32 v18, 12, v45
	s_lshl_b32 s1, s3, 12
	v_lshl_or_b32 v95, v19, 4, v72
	v_bitop3_b32 v19, v45, v79, 8 bitop3:0x36
	v_bitop3_b32 v18, v10, v18, v3 bitop3:0x36
	s_ashr_i32 s0, s0, 7
	s_add_i32 s1, s1, 0
	v_lshl_or_b32 v97, v19, 4, v72
	v_bitop3_b32 v19, v45, v79, 10 bitop3:0x36
	v_lshl_or_b32 v102, v18, 4, v75
	v_or_b32_e32 v18, 14, v45
	s_cmp_gt_i32 s0, -1
	v_or_b32_e32 v80, v10, v3
	v_lshl_or_b32 v99, v19, 4, v72
	v_bitop3_b32 v19, v45, v79, 12 bitop3:0x36
	v_bitop3_b32 v3, v10, v18, v3 bitop3:0x36
	v_lshlrev_b32_e32 v10, 2, v67
	s_cselect_b64 s[74:75], -1, 0
	s_cmp_gt_i32 s0, 0
	v_lshl_or_b32 v101, v19, 4, v72
	v_bitop3_b32 v19, v45, v79, 14 bitop3:0x36
	v_lshl_or_b32 v104, v3, 4, v75
	v_bfe_u32 v3, v67, 4, 2
	v_and_b32_e32 v10, 12, v10
	s_cselect_b64 s[82:83], -1, 0
	s_cmp_gt_i32 s0, 1
	s_mov_b64 s[70:71], 0x3a600000
	v_lshl_or_b32 v103, v19, 4, v72
	v_lshl_add_u32 v18, v68, 8, s1
	v_bitop3_b32 v19, v10, v3, v5 bitop3:0x36
	v_or_b32_e32 v20, 4, v3
	s_cselect_b64 s[84:85], -1, 0
	v_or_b32_e32 v21, 8, v3
	s_cmp_gt_i32 s0, 2
	v_or_b32_e32 v3, 12, v3
	v_lshl_or_b32 v105, s3, 4, v68
	s_movk_i32 s33, 0x210
	s_mov_b64 s[0:1], 0x38600000
	v_writelane_b32 v254, s4, 10
	v_lshl_add_u64 v[48:49], v[6:7], 0, s[70:71]
	v_bitop3_b32 v20, v10, v20, v5 bitop3:0x36
	v_bitop3_b32 v21, v10, v21, v5 bitop3:0x36
	s_cselect_b64 s[86:87], -1, 0
	v_bitop3_b32 v3, v10, v3, v5 bitop3:0x36
	v_mul_lo_u32 v5, v105, s33
	s_add_i32 s70, 0, 0x10400
	v_lshl_add_u64 v[54:55], v[6:7], 0, s[0:1]
	s_mov_b64 s[0:1], 0x51000000
	v_writelane_b32 v254, s5, 11
	v_lshlrev_b32_e32 v36, 7, v1
	v_cmp_gt_i32_e64 s[14:15], v8, v1
	v_lshlrev_b32_e32 v13, 8, v1
	v_lshlrev_b32_e32 v38, 7, v69
	v_cmp_gt_i32_e64 s[30:31], v8, v69
	v_lshlrev_b32_e32 v14, 8, v69
	v_lshl_add_u32 v15, v15, 4, 0
	v_lshlrev_b32_e32 v40, 7, v73
	v_cmp_gt_i32_e64 s[48:49], v8, v73
	v_lshlrev_b32_e32 v16, 8, v73
	v_lshl_add_u32 v17, v17, 4, 0
	v_lshlrev_b32_e32 v42, 7, v76
	v_cmp_gt_i32_e64 s[64:65], v8, v76
	v_lshlrev_b32_e32 v8, 8, v76
	v_add_u32_e32 v84, 32, v1
	v_add_u32_e32 v83, 64, v1
	v_add_u32_e32 v82, 0x60, v1
	v_lshlrev_b32_e32 v19, 4, v19
	v_lshlrev_b32_e32 v20, 4, v20
	v_lshlrev_b32_e32 v21, 4, v21
	v_lshlrev_b32_e32 v3, 4, v3
	v_add_u32_e32 v5, s70, v5
	v_and_b32_e32 v10, 48, v67
	v_add_u32_e32 v4, s70, v4
	v_lshl_add_u64 v[56:57], v[6:7], 0, s[0:1]
	v_mul_lo_u32 v6, v1, s33
	s_lshl_b32 s33, s92, 4
	s_mov_b32 s0, s92
	v_ashrrev_i32_e32 v37, 31, v36
	v_cmp_gt_i32_e64 s[20:21], v11, v1
	v_cmp_gt_i32_e64 s[22:23], v12, v1
	s_mov_b32 s77, 0
	v_ashrrev_i32_e32 v39, 31, v38
	v_cmp_gt_i32_e64 s[38:39], v11, v69
	v_cmp_gt_i32_e64 s[40:41], v12, v69
	v_ashrrev_i32_e32 v41, 31, v40
	v_cmp_gt_i32_e64 s[54:55], v11, v73
	v_cmp_gt_i32_e64 s[56:57], v12, v73
	v_ashrrev_i32_e32 v43, 31, v42
	v_lshlrev_b32_e32 v85, 3, v1
	v_lshlrev_b32_e32 v86, 3, v84
	v_lshlrev_b32_e32 v70, 8, v84
	v_lshlrev_b32_e32 v87, 3, v83
	v_lshlrev_b32_e32 v71, 8, v83
	v_lshlrev_b32_e32 v88, 3, v82
	v_lshlrev_b32_e32 v74, 8, v82
	s_movk_i32 s4, 0x80
	s_movk_i32 s90, 0x800
	v_mov_b32_e32 v106, 0x260
	v_add_u32_e32 v107, v15, v14
	v_add_u32_e32 v108, v17, v16
	v_add_u32_e32 v109, v9, v8
	v_add_u32_e32 v110, v18, v19
	v_add_u32_e32 v111, v18, v20
	v_add_u32_e32 v112, v18, v21
	v_add_u32_e32 v113, v18, v3
	v_add_u32_e32 v114, v5, v10
	v_add_u32_e32 v115, v4, v6
	v_add_u32_e32 v66, v81, v13
	s_mov_b32 s91, s33
	v_writelane_b32 v254, s0, 12
	v_cmp_gt_i32_e64 s[70:71], v11, v76
	v_cmp_gt_i32_e64 s[72:73], v12, v76
	v_writelane_b32 v254, s1, 13
	s_movk_i32 s100, 0x380
	s_cmpk_lt_i32 s92, 0x80
	s_cbranch_scc1 .Lp2_sp_go
	s_movk_i32 s100, 0x400
	s_addk_i32 s92, 0x300
	s_lshl_b32 s91, s92, 4
